# N2: x rows prefetched two 16-row groups ahead (two register buffers chosen by group parity, uniform load counts, counted vmcnt)
# baseline (speedup 1.0000x reference)
; #define GAS __attribute__((address_space(1)))
; #define LAS __attribute__((address_space(3)))
; __device__ __forceinline__ void n2_phase(const Frame& F0, int L, int nrows) {
;     ...
;     { const GAS u32x4* img = (const GAS u32x4*)(F.ws + WS_RIMG + (size_t)L * 65536) + F.tid;
;       u32x4 iv[8];
; #pragma unroll
;       for (int i = 0; i < 8; ++i) iv[i] = img[512 * i];
; #pragma unroll
;       for (int i = 0; i < 8; ++i) *((LAS u32x4*)WH + F.tid + 512 * i) = iv[i]; }
;     __syncthreads();
;     const float* gn = inp(F, I_N2G) + L * 1024; const float* modL = (const float*)(F.ws + WS_MOD) + (size_t)L * 17 * 6144;
;     unsigned char* H8 = F.ws + WS_H; float* AFF = (float*)(F.ws + WS_AFF); const bf16_t* X = (const bf16_t*)(F.ws + WS_X);
;     const int RPB = nrows / F.G, NG = RPB / 16, rb = (int)blockIdx.x * RPB;
;     const int r = F.lane & 15, kg = F.lane >> 4, c0 = 128 * F.wave + 8 * kg;
;     u32x4 nraw[4];
; #pragma unroll
;     for (int s_ = 0; s_ < 4; ++s_) nraw[s_] = *(const GAS u32x4*)(X + (size_t)(rb + r) * D + c0 + 32 * s_);
.LBB0_1200:
	s_andn2_b64 vcc, exec, s[0:1]
	s_cbranch_vccnz .LBB0_1268
	v_readlane_b32 s0, v255, 17
	v_readlane_b32 s1, v255, 18
	s_lshl_b64 s[0:1], s[0:1], 16
	v_readlane_b32 s2, v254, 5
	s_waitcnt vmcnt(0) lgkmcnt(0)
	v_mov_b32_e32 v18, v0
	s_add_u32 s0, s2, s0
	v_readlane_b32 s2, v254, 6
	s_addc_u32 s1, s2, s1
	v_ashrrev_i32_e32 v19, 31, v18
	v_lshl_add_u64 v[28:29], v[18:19], 4, s[0:1]
	s_movk_i32 s0, 0x2000
	v_add_co_u32_e32 v6, vcc, s0, v28
	s_movk_i32 s0, 0x4000
	s_nop 0
	v_addc_co_u32_e32 v7, vcc, 0, v29, vcc
	v_add_co_u32_e32 v10, vcc, s0, v28
	s_movk_i32 s0, 0x6000
	s_nop 0
	v_addc_co_u32_e32 v11, vcc, 0, v29, vcc
	v_add_co_u32_e32 v14, vcc, s0, v28
	s_mov_b32 s0, 0x8000
	s_nop 0
	v_addc_co_u32_e32 v15, vcc, 0, v29, vcc
	v_add_co_u32_e32 v20, vcc, s0, v28
	s_mov_b32 s0, 0xa000
	s_nop 0
	v_addc_co_u32_e32 v21, vcc, 0, v29, vcc
	v_add_co_u32_e32 v24, vcc, s0, v28
	s_mov_b32 s0, 0xc000
	s_nop 0
	v_addc_co_u32_e32 v25, vcc, 0, v29, vcc
	v_add_co_u32_e32 v30, vcc, s0, v28
	s_mov_b32 s0, 0xe000
	s_nop 0
	v_addc_co_u32_e32 v31, vcc, 0, v29, vcc
	v_add_co_u32_e32 v32, vcc, s0, v28
	global_load_dwordx4 v[2:5], v[28:29], off
	s_nop 0
	global_load_dwordx4 v[6:9], v[6:7], off
	v_addc_co_u32_e32 v33, vcc, 0, v29, vcc
	global_load_dwordx4 v[10:13], v[10:11], off
	s_nop 0
	global_load_dwordx4 v[14:17], v[14:15], off
	s_nop 0
	global_load_dwordx4 v[20:23], v[20:21], off
	s_nop 0
	global_load_dwordx4 v[24:27], v[24:25], off
	s_nop 0
	global_load_dwordx4 v[28:31], v[30:31], off
	s_nop 0
	global_load_dwordx4 v[32:35], v[32:33], off
	v_readlane_b32 s0, v255, 10
	v_readlane_b32 s3, v255, 16
	v_readlane_b32 s5, v254, 60
	v_mov_b32_e32 v1, s0
	v_readlane_b32 s0, v254, 61
	s_mul_hi_u32 s1, s3, s0
	s_mul_i32 s2, s1, s5
	s_sub_i32 s2, s3, s2
	s_add_i32 s3, s1, 1
	s_sub_i32 s4, s2, s5
	s_cmp_ge_u32 s2, s5
	v_lshl_add_u32 v19, v18, 4, 0
	s_cselect_b32 s1, s3, s1
	s_cselect_b32 s2, s4, s2
	s_add_i32 s3, s1, 1
	s_cmp_ge_u32 s2, s5
	s_cselect_b32 s1, s3, s1
	v_readlane_b32 s2, v252, 10
	s_xor_b32 s1, s1, s2
	s_sub_i32 s3, s1, s2
	v_readfirstlane_b32 s0, v18
	s_cmp_lt_i32 s3, 16
	s_waitcnt vmcnt(7)
	ds_write_b128 v19, v[2:5]
	s_waitcnt vmcnt(3)
	ds_write_b128 v19, v[20:23] offset:32768
	ds_write_b128 v19, v[6:9] offset:8192
	ds_write_b128 v19, v[10:13] offset:16384
	ds_write_b128 v19, v[14:17] offset:24576
	s_waitcnt vmcnt(2)
	ds_write_b128 v19, v[24:27] offset:40960
	s_waitcnt vmcnt(1)
	ds_write_b128 v19, v[28:31] offset:49152
	s_waitcnt vmcnt(0)
	ds_write_b128 v19, v[32:35] offset:57344
	s_waitcnt lgkmcnt(0)
	s_barrier
	ds_read_b64 v[2:3], v1
	s_waitcnt lgkmcnt(0)
	v_readfirstlane_b32 s1, v2
	v_readfirstlane_b32 s2, v3
	s_cbranch_scc1 .LBB0_1214
	s_mul_i32 s4, s3, s84
	v_and_b32_e32 v26, 15, v18
	v_bfe_u32 v27, v18, 4, 2
	s_ashr_i32 s8, s0, 6
	v_lshlrev_b32_e32 v1, 3, v27
	v_add_u32_e32 v82, s4, v26
	v_lshl_or_b32 v20, s8, 7, v1
	v_ashrrev_i32_e32 v83, 31, v82
	v_readlane_b32 s10, v252, 20
	v_ashrrev_i32_e32 v21, 31, v20
	v_lshlrev_b64 v[2:3], 11, v[82:83]
	v_readlane_b32 s11, v252, 21
	v_lshlrev_b64 v[22:23], 1, v[20:21]
	s_ashr_i32 s5, s3, 31
	v_lshl_add_u64 v[2:3], s[10:11], 0, v[2:3]
	v_lshl_add_u64 v[2:3], v[2:3], 0, v[22:23]
	global_load_dwordx4 v[14:17], v[2:3], off offset:192
	global_load_dwordx4 v[10:13], v[2:3], off offset:128
	global_load_dwordx4 v[6:9], v[2:3], off offset:64
	s_nop 0
	global_load_dwordx4 v[2:5], v[2:3], off
	s_lshr_b32 s5, s5, 28
	v_readlane_b32 s6, v255, 17
	s_add_i32 s3, s3, s5
	v_readlane_b32 s7, v255, 18
	s_lshl_b32 s12, s6, 10
	s_ashr_i32 s5, s3, 4
	s_lshl_b64 s[6:7], s[12:13], 2
	s_add_u32 s6, s1, s6
	s_addc_u32 s7, s2, s7
	s_add_i32 s1, 0, 0x10000
	v_lshlrev_b32_e32 v190, 2, v26
	s_andn2_b32 s0, s0, 63
	v_and_b32_e32 v18, 63, v18
	v_add_u32_e32 v1, s1, v190
	s_add_i32 s0, s0, s1
	v_lshlrev_b32_e32 v28, 8, v27
	v_readlane_b32 s1, v255, 11
	v_lshl_add_u64 v[84:85], s[10:11], 0, v[22:23]
	v_add_u32_e32 v230, 16, v82
	v_ashrrev_i32_e32 v231, 31, v230
	v_lshlrev_b64 v[230:231], 11, v[230:231]
	v_lshl_add_u64 v[230:231], v[84:85], 0, v[230:231]
	global_load_dwordx4 v[214:217], v[230:231], off
	global_load_dwordx4 v[218:221], v[230:231], off offset:64
	global_load_dwordx4 v[222:225], v[230:231], off offset:128
	global_load_dwordx4 v[226:229], v[230:231], off offset:192
	v_cmp_gt_u32_e64 s[36:37], 16, v18
	v_lshl_add_u32 v83, v18, 2, s0
	v_add_u32_e32 v29, s1, v190
	v_cmp_gt_u32_e64 s[38:39], 32, v18
	s_lshl_b32 s1, s8, 1
	v_readlane_b32 s2, v254, 7
	v_or_b32_e32 v18, 32, v20
	v_or_b32_e32 v22, 64, v20
	v_or_b32_e32 v24, 0x60, v20
	v_lshl_or_b32 v31, s8, 12, v28
	s_lshl_b32 s0, s8, 10
	v_add_u32_e32 v30, s1, v27
	v_readlane_b32 s3, v254, 8
	v_ashrrev_i32_e32 v19, 31, v18
	v_or_b32_e32 v92, 36, v20
	v_ashrrev_i32_e32 v23, 31, v22
	v_or_b32_e32 v94, 0x44, v20
	v_ashrrev_i32_e32 v25, 31, v24
	v_or_b32_e32 v96, 0x64, v20
	v_lshl_or_b32 v26, v26, 4, v31
	s_add_i32 s1, s1, s4
	v_lshl_add_u64 v[86:87], s[96:97], 0, v[20:21]
	v_lshl_add_u64 v[88:89], s[2:3], 0, v[190:191]
	v_lshl_add_u64 v[90:91], v[20:21], 2, s[6:7]
	v_ashrrev_i32_e32 v93, 31, v92
	v_ashrrev_i32_e32 v95, 31, v94
	v_ashrrev_i32_e32 v97, 31, v96
	v_add_u32_e32 v143, 0, v26
	v_lshl_add_u32 v156, v30, 6, v29
	v_add3_u32 v157, v29, s0, v28
	v_add_u32_e32 v158, s1, v27
	s_mov_b32 s7, 0
	v_lshlrev_b64 v[98:99], 2, v[20:21]
	v_lshlrev_b64 v[100:101], 2, v[18:19]
	v_lshlrev_b64 v[102:103], 2, v[22:23]
	v_lshlrev_b64 v[104:105], 2, v[24:25]
	s_branch .LBB0_1204

; #define GAS __attribute__((address_space(1)))
; __device__ __forceinline__ void n2_phase(const Frame& F0, int L, int nrows) {
;     ...
;     for (int g = 0; g < NG;) {
;       int gend = NG;
;       { const int row0_ = rb + 16 * g, bm = row0_ < NLAT ? (row0_ >> 11) : 16; const float* mrow = modL + bm * 6144;
;         if (row0_ < NLAT) { const int ge = ((((row0_ >> 11) + 1) << 11) - rb) >> 4; gend = ge < NG ? ge : NG; }
; #pragma unroll
;         for (int s_ = 0; s_ < 4; ++s_)
; #pragma unroll
;             for (int q = 0; q < 2; ++q) { const int c = c0 + 32 * s_ + 4 * q; gs[s_][q] = *(const GAS f32x4*)(gn + c) * (*(const GAS f32x4*)(mrow + 4 * 1024 + c) + 1.0f); sh[s_][q] = *(const GAS f32x4*)(mrow + 3 * 1024 + c); } }
;       for (; g < gend; ++g) {
;         const int row0 = rb + 16 * g, row = row0 + r, par = g & 1;
;         f32x4 v[4][2];
; #pragma unroll
;         for (int s_ = 0; s_ < 4; ++s_) { v[s_][0] = (f32x4){bf_lo(nraw[s_].x), bf_hi(nraw[s_].x), bf_lo(nraw[s_].y), bf_hi(nraw[s_].y)}; v[s_][1] = (f32x4){bf_lo(nraw[s_].z), bf_hi(nraw[s_].z), bf_lo(nraw[s_].w), bf_hi(nraw[s_].w)}; }
;         if (g + 1 < NG) {
; #pragma unroll
;             for (int s_ = 0; s_ < 4; ++s_) nraw[s_] = *(const GAS u32x4*)(X + (size_t)(row + 16) * D + c0 + 32 * s_);
;         }
;         float ss = 0.f;
; #pragma unroll
;         for (int s_ = 0; s_ < 4; ++s_)
; #pragma unroll
;             for (int q = 0; q < 2; ++q) ss += (v[s_][q][0] * v[s_][q][0] + v[s_][q][1] * v[s_][q][1]) + (v[s_][q][2] * v[s_][q][2] + v[s_][q][3] * v[s_][q][3]);
;         ss += __shfl_xor(ss, 16); ss += __shfl_xor(ss, 32);
.LBB0_1204:
	s_lshl_b32 s8, s7, 4
	s_add_i32 s2, s8, s4
	s_and_b32 s0, s2, 0xfffff800
	s_sub_i32 s0, s0, s4
	s_addk_i32 s0, 0x800
	s_ashr_i32 s0, s0, 4
	s_min_i32 s3, s0, s5
	s_cmp_lt_i32 s2, 0x8000
	s_cselect_b64 s[0:1], -1, 0
	s_and_b64 s[10:11], s[0:1], exec
	s_cselect_b32 s6, s3, s5
	s_cmp_ge_i32 s7, s6
	s_cbranch_scc1 .LBB0_1203
	s_lshr_b32 s2, s2, 11
	s_mulk_i32 s2, 0x1800
	s_and_b64 s[0:1], s[0:1], exec
	s_cselect_b32 s0, s2, 0x18000
	s_ashr_i32 s1, s0, 31
	s_lshl_b64 s[0:1], s[0:1], 2
	s_add_u32 s2, s46, s0
	s_addc_u32 s3, s47, s1
	s_add_u32 s0, s2, 0x4000
	s_addc_u32 s1, s3, 0
	s_add_u32 s2, s2, 0x3000
	s_addc_u32 s3, s3, 0
	global_load_dwordx4 v[106:109], v[90:91], off
	global_load_dwordx4 v[110:113], v[90:91], off offset:16
	global_load_dwordx4 v[114:117], v[90:91], off offset:128
	global_load_dwordx4 v[118:121], v[90:91], off offset:144
	global_load_dwordx4 v[122:125], v[90:91], off offset:256
	global_load_dwordx4 v[126:129], v[90:91], off offset:272
	global_load_dwordx4 v[130:133], v[90:91], off offset:384
	global_load_dwordx4 v[134:137], v[90:91], off offset:400
	v_lshl_add_u64 v[50:51], s[0:1], 0, v[98:99]
	v_lshl_add_u64 v[58:59], s[0:1], 0, v[100:101]
	v_lshl_add_u64 v[62:63], v[92:93], 2, s[0:1]
	v_lshl_add_u64 v[66:67], s[0:1], 0, v[102:103]
	v_lshl_add_u64 v[70:71], v[94:95], 2, s[0:1]
	v_lshl_add_u64 v[74:75], s[0:1], 0, v[104:105]
	v_lshl_add_u64 v[78:79], v[96:97], 2, s[0:1]
	global_load_dwordx4 v[54:57], v[50:51], off offset:16
	s_nop 0
	global_load_dwordx4 v[50:53], v[50:51], off
	global_load_dwordx4 v[58:61], v[58:59], off
	global_load_dwordx4 v[62:65], v[62:63], off
	global_load_dwordx4 v[66:69], v[66:67], off
	global_load_dwordx4 v[70:73], v[70:71], off
	global_load_dwordx4 v[74:77], v[74:75], off
	global_load_dwordx4 v[78:81], v[78:79], off
	v_lshl_add_u64 v[22:23], s[2:3], 0, v[98:99]
	global_load_dwordx4 v[18:21], v[22:23], off offset:16
	s_nop 0
	global_load_dwordx4 v[22:25], v[22:23], off
	v_lshl_add_u64 v[30:31], s[2:3], 0, v[100:101]
	global_load_dwordx4 v[26:29], v[30:31], off offset:16
	s_nop 0
	global_load_dwordx4 v[30:33], v[30:31], off
	v_lshl_add_u64 v[38:39], s[2:3], 0, v[102:103]
	global_load_dwordx4 v[34:37], v[38:39], off offset:16
	s_nop 0
	global_load_dwordx4 v[38:41], v[38:39], off
	v_lshl_add_u64 v[46:47], s[2:3], 0, v[104:105]
	global_load_dwordx4 v[42:45], v[46:47], off offset:16
	s_nop 0
	global_load_dwordx4 v[46:49], v[46:47], off
	v_add_u32_e32 v138, s8, v158
	v_add_u32_e32 v140, s8, v82
	s_waitcnt vmcnt(0)
	v_pk_add_f32 v[50:51], v[50:51], 1.0 op_sel_hi:[1,0]
	v_pk_add_f32 v[52:53], v[52:53], 1.0 op_sel_hi:[1,0]
	v_pk_add_f32 v[54:55], v[54:55], 1.0 op_sel_hi:[1,0]
	v_pk_add_f32 v[56:57], v[56:57], 1.0 op_sel_hi:[1,0]
	v_pk_add_f32 v[58:59], v[58:59], 1.0 op_sel_hi:[1,0]
	v_pk_add_f32 v[60:61], v[60:61], 1.0 op_sel_hi:[1,0]
	v_pk_add_f32 v[62:63], v[62:63], 1.0 op_sel_hi:[1,0]
	v_pk_add_f32 v[64:65], v[64:65], 1.0 op_sel_hi:[1,0]
	v_pk_add_f32 v[66:67], v[66:67], 1.0 op_sel_hi:[1,0]
	v_pk_add_f32 v[68:69], v[68:69], 1.0 op_sel_hi:[1,0]
	v_pk_add_f32 v[70:71], v[70:71], 1.0 op_sel_hi:[1,0]
	v_pk_add_f32 v[72:73], v[72:73], 1.0 op_sel_hi:[1,0]
	v_pk_add_f32 v[74:75], v[74:75], 1.0 op_sel_hi:[1,0]
	v_pk_add_f32 v[76:77], v[76:77], 1.0 op_sel_hi:[1,0]
	v_pk_add_f32 v[78:79], v[78:79], 1.0 op_sel_hi:[1,0]
	v_pk_add_f32 v[80:81], v[80:81], 1.0 op_sel_hi:[1,0]
	v_pk_mul_f32 v[50:51], v[106:107], v[50:51]
	v_pk_mul_f32 v[106:107], v[108:109], v[52:53]
	v_pk_mul_f32 v[54:55], v[110:111], v[54:55]
	v_pk_mul_f32 v[110:111], v[112:113], v[56:57]
	v_pk_mul_f32 v[58:59], v[114:115], v[58:59]
	v_pk_mul_f32 v[114:115], v[116:117], v[60:61]
	v_pk_mul_f32 v[62:63], v[118:119], v[62:63]
	v_pk_mul_f32 v[118:119], v[120:121], v[64:65]
	v_pk_mul_f32 v[66:67], v[122:123], v[66:67]
	v_pk_mul_f32 v[122:123], v[124:125], v[68:69]
	v_pk_mul_f32 v[70:71], v[126:127], v[70:71]
	v_pk_mul_f32 v[126:127], v[128:129], v[72:73]
	v_pk_mul_f32 v[74:75], v[130:131], v[74:75]
	v_pk_mul_f32 v[130:131], v[132:133], v[76:77]
	v_pk_mul_f32 v[78:79], v[134:135], v[78:79]
	v_pk_mul_f32 v[134:135], v[136:137], v[80:81]
	v_mov_b64_e32 v[108:109], v[50:51]
	v_mov_b64_e32 v[112:113], v[54:55]
	v_mov_b64_e32 v[116:117], v[58:59]
	v_mov_b64_e32 v[120:121], v[62:63]
	v_mov_b64_e32 v[124:125], v[66:67]
	v_mov_b64_e32 v[128:129], v[70:71]
	v_mov_b64_e32 v[132:133], v[74:75]
	v_mov_b64_e32 v[136:137], v[78:79]
	v_and_b32_e32 v51, 64, v211
	v_add_u32_e32 v51, 64, v51
	v_xor_b32_e32 v50, 16, v211
	v_cmp_lt_i32_e32 vcc, v50, v51
	s_nop 1
	v_cndmask_b32_e32 v50, v211, v50, vcc
	v_lshlrev_b32_e32 v159, 2, v50
	v_xor_b32_e32 v50, 32, v211
	v_cmp_lt_i32_e32 vcc, v50, v51
	s_nop 1
	v_cndmask_b32_e32 v50, v211, v50, vcc
	v_lshlrev_b32_e32 v160, 2, v50
	v_xor_b32_e32 v50, 1, v211
	v_cmp_lt_i32_e32 vcc, v50, v51
	s_nop 1
	v_cndmask_b32_e32 v50, v211, v50, vcc
	v_lshlrev_b32_e32 v161, 2, v50
	v_xor_b32_e32 v50, 2, v211
	v_cmp_lt_i32_e32 vcc, v50, v51
	s_nop 1
	v_cndmask_b32_e32 v50, v211, v50, vcc
	v_lshlrev_b32_e32 v162, 2, v50
	v_xor_b32_e32 v50, 4, v211
	v_cmp_lt_i32_e32 vcc, v50, v51
	s_nop 1
	v_cndmask_b32_e32 v50, v211, v50, vcc
	v_lshlrev_b32_e32 v163, 2, v50
	v_xor_b32_e32 v50, 8, v211
	v_cmp_lt_i32_e32 vcc, v50, v51
	s_nop 1
	v_cndmask_b32_e32 v50, v211, v50, vcc
	v_lshlrev_b32_e32 v164, 2, v50
	s_branch .Ln2_top_common
.LBB0_1206:
	s_waitcnt vmcnt(14)
	v_mov_b32_e32 v140, v165
	s_mov_b32 s7, s2
.Ln2_top_common:
	s_add_i32 s2, s7, 1
	v_add_u32_e32 v165, 16, v140
	s_add_i32 s0, s7, 2
	s_add_i32 s1, s5, -1
	s_min_i32 s0, s0, s1
	s_lshl_b32 s0, s0, 4
	v_add_u32_e32 v230, s0, v82
	v_ashrrev_i32_e32 v231, 31, v230
	v_lshlrev_b64 v[230:231], 11, v[230:231]
	v_lshl_add_u64 v[230:231], v[84:85], 0, v[230:231]
	s_bitcmp1_b32 s7, 0
	s_cbranch_scc1 .Ln2_odd
	v_mov_b64_e32 v[64:65], v[4:5]
	v_mov_b64_e32 v[60:61], v[8:9]
	v_mov_b64_e32 v[56:57], v[12:13]
	v_mov_b64_e32 v[52:53], v[16:17]
	v_mov_b64_e32 v[62:63], v[2:3]
	v_mov_b64_e32 v[58:59], v[6:7]
	v_mov_b64_e32 v[54:55], v[10:11]
	v_mov_b64_e32 v[50:51], v[14:15]
	global_load_dwordx4 v[2:5], v[230:231], off
	global_load_dwordx4 v[6:9], v[230:231], off offset:64
	global_load_dwordx4 v[10:13], v[230:231], off offset:128
	global_load_dwordx4 v[14:17], v[230:231], off offset:192
	s_branch .LBB0_1208
.Ln2_odd:
	v_mov_b64_e32 v[64:65], v[216:217]
	v_mov_b64_e32 v[60:61], v[220:221]
	v_mov_b64_e32 v[56:57], v[224:225]
	v_mov_b64_e32 v[52:53], v[228:229]
	v_mov_b64_e32 v[62:63], v[214:215]
	v_mov_b64_e32 v[58:59], v[218:219]
	v_mov_b64_e32 v[54:55], v[222:223]
	v_mov_b64_e32 v[50:51], v[226:227]
	global_load_dwordx4 v[214:217], v[230:231], off
	global_load_dwordx4 v[218:221], v[230:231], off offset:64
	global_load_dwordx4 v[222:225], v[230:231], off offset:128
	global_load_dwordx4 v[226:229], v[230:231], off offset:192
